# baseline (speedup 1.0000x reference)
_Z9k_redprepILi1EEvPKfPKjS1_S1_S1_S1_S1_PfPKDv8_DF16_S7_S1_PDF16_S4_S4_S4_PKiS7_S1_S1_S1_S4_S4_:
	s_load_dwordx8 s[4:11], s[0:1], 0x8
	v_readfirstlane_b32 s3, v0
	s_lshr_b32 s3, s3, 6
	s_cmp_ge_u32 s3, 4
	s_cbranch_scc1 .Lmy_prio1_done
	s_setprio 1

.LBB4_2:
	s_or_b64 exec, exec, s[4:5]
	s_lshr_b32 s3, s84, 6
	s_cmp_ge_u32 s3, 4
	s_cbranch_scc1 .Lmy_prio2_done
	s_setprio 1
